# speedup vs baseline: 1.0753x; 1.0068x over previous
_Z5k_csrPKjPKiS2_PiPKfPfPDF16_S3_S3_S3_S5_S5_S5_S5_S7_S6_:
	s_lshl_b32 s3, s2, 6
	s_and_b32 s33, s3, 0x1c0
	s_lshr_b32 s2, s2, 3
	s_add_i32 s33, s33, s2
	s_cmpk_lt_u32 s33, 0x1df
	s_mov_b64 s[2:3], -1
	s_cbranch_scc0 .LBB1_243
	s_mul_i32 s48, s33, 0xd1
	s_sub_i32 s2, 0x186a0, s48
	s_min_u32 s62, s2, 0xd1
	s_lshl_b32 s6, s62, 2
	s_mov_b32 s49, 0
	v_cmp_gt_u32_e64 s[2:3], s6, v0
	v_mov_b32_e32 v1, 0
	v_mov_b32_e32 v21, 0
	v_mov_b32_e32 v20, 0
	v_mov_b32_e32 v22, 0
	s_and_saveexec_b64 s[4:5], s[2:3]
	s_cbranch_execz .LBB1_3
	s_load_dwordx2 s[8:9], s[0:1], 0x20
	s_add_i32 s10, s6, -1
	s_lshl_b64 s[6:7], s[48:49], 5
	v_min_u32_e32 v1, s10, v0
	v_lshlrev_b32_e32 v1, 3, v1
	s_waitcnt lgkmcnt(0)
	s_add_u32 s6, s8, s6
	s_addc_u32 s7, s9, s7
	global_load_dwordx2 v[20:21], v1, s[6:7]

.LBB1_8:
	s_or_b64 exec, exec, s[4:5]
	v_lshrrev_b32_e32 v23, 5, v0
	v_lshlrev_b32_e32 v10, 2, v23
	s_waitcnt lgkmcnt(0)
	s_barrier
	ds_read2st64_b32 v[8:9], v10 offset0:128 offset1:132
	v_mov_b32_e32 v7, 0
	ds_read_b32 v25, v7 offset:38932
	v_mul_u32_u24_e32 v6, 0xc350, v23
	v_and_b32_e32 v24, 31, v0
	v_lshl_add_u64 v[2:3], s[50:51], 0, v[6:7]
	s_waitcnt lgkmcnt(1)
	v_ashrrev_i32_e32 v5, 31, v8
	v_mov_b32_e32 v4, v8
	v_lshl_add_u64 v[4:5], v[4:5], 2, v[2:3]
	v_cmp_lt_i32_e32 vcc, v24, v9
	v_mov_b32_e32 v28, -1
	v_or_b32_e32 v31, 0x8400, v10
	v_or_b32_e32 v30, 0x8000, v10
	v_or_b32_e32 v29, 32, v24
	v_mov_b32_e32 v10, -1
	v_mov_b32_e32 v11, -1
	s_and_saveexec_b64 s[4:5], vcc
	s_cbranch_execz .LBB1_10
	v_lshlrev_b32_e32 v12, 2, v24
	v_mov_b32_e32 v13, v7
	v_lshl_add_u64 v[12:13], v[4:5], 0, v[12:13]
	global_load_dword v10, v[12:13], off
.LBB1_10:
	s_or_b64 exec, exec, s[4:5]
	v_cmp_lt_i32_e32 vcc, v29, v9
	s_and_saveexec_b64 s[4:5], vcc
	s_cbranch_execz .LBB1_12
	v_lshlrev_b32_e32 v12, 2, v24
	v_mov_b32_e32 v13, 0
	v_lshl_add_u64 v[4:5], v[4:5], 0, v[12:13]
	global_load_dword v28, v[4:5], off offset:128
.LBB1_12:
	s_or_b64 exec, exec, s[4:5]
	ds_read_b32 v7, v31 offset:128
	ds_read_b32 v12, v30 offset:128
	s_mov_b64 s[4:5], 0x186a00
	v_lshl_add_u64 v[4:5], v[2:3], 0, s[4:5]
	v_mov_b32_e32 v9, -1
	v_mov_b32_e32 v19, 0
	s_waitcnt lgkmcnt(0)
	v_ashrrev_i32_e32 v13, 31, v12
	v_lshl_add_u64 v[2:3], v[12:13], 2, v[4:5]
	v_cmp_lt_i32_e32 vcc, v24, v7
	s_and_saveexec_b64 s[4:5], vcc
	s_cbranch_execz .LBB1_14
	v_lshlrev_b32_e32 v18, 2, v24
	v_lshl_add_u64 v[12:13], v[2:3], 0, v[18:19]
	global_load_dword v11, v[12:13], off

.LBB1_38:
	s_or_b64 exec, exec, s[4:5]
	v_cmp_lt_i32_e32 vcc, v29, v8
	v_mov_b32_e32 v8, -1
	s_and_saveexec_b64 s[4:5], vcc
	s_cbranch_execnz .LBB1_246
	s_or_b64 exec, exec, s[4:5]
	s_waitcnt vmcnt(0)
	v_cmp_ne_u32_e64 s[42:43], -1, v10
	s_and_saveexec_b64 s[4:5], s[42:43]
	s_cbranch_execnz .LBB1_247

.LBB1_231:
	s_and_saveexec_b64 s[4:5], s[2:3]
	s_cbranch_execz .LBB1_233
	v_cvt_f32_f16_e32 v1, v20
	v_cvt_f32_f16_sdwa v22, v21 dst_sel:DWORD dst_unused:UNUSED_PAD src0_sel:WORD_1
	v_cvt_f32_f16_sdwa v4, v20 dst_sel:DWORD dst_unused:UNUSED_PAD src0_sel:WORD_1
	v_cvt_f32_f16_e32 v20, v21
	s_nop 0
	v_mov_b32_e32 v21, v4
	v_and_b32_e32 v2, 0x3fc, v0
	ds_read_b32 v2, v2 offset:36864
	v_mov_b32_e32 v3, 0
	s_lshl_b64 s[2:3], s[48:49], 4
	s_add_u32 s2, s54, s2
	s_addc_u32 s3, s55, s3
	s_waitcnt lgkmcnt(0)
	v_mul_f32_e32 v2, 0x41800000, v2
	v_mul_f32_e32 v1, v1, v2
	v_mul_f32_e32 v4, v21, v2
	v_cvt_pk_fp8_f32 v3, v1, v4
	v_mul_f32_e32 v1, v20, v2
	v_mul_f32_e32 v2, v22, v2
	v_cvt_pk_fp8_f32 v3, v1, v2 op_sel:[0,0,1]
	v_lshlrev_b32_e32 v1, 2, v0
	global_store_dword v1, v3, s[2:3]

.LBB1_246:
	v_lshlrev_b32_e32 v14, 2, v24
	v_mov_b32_e32 v15, 0
	v_lshl_add_u64 v[12:13], v[12:13], 0, v[14:15]
	global_load_dword v8, v[12:13], off offset:128
	s_or_b64 exec, exec, s[4:5]
	s_waitcnt vmcnt(0)
	v_cmp_ne_u32_e64 s[42:43], -1, v10
	s_and_saveexec_b64 s[4:5], s[42:43]
	s_cbranch_execz .LBB1_40
